# baseline (speedup 1.0000x reference)
.LBB1_18:
	s_lshl_b64 s[6:7], s[10:11], 20
	s_add_u32 s3, s12, s6
	s_addc_u32 s5, s13, s7
	s_lshl_b32 s10, s2, 2
	v_lshlrev_b32_e32 v0, 7, v194
	s_add_u32 s10, s3, s10
	v_and_b32_e32 v0, 0xfffffc00, v0
	s_addc_u32 s11, s5, 0
	v_ashrrev_i32_e32 v1, 31, v0
	v_lshl_add_u64 v[2:3], v[0:1], 2, s[10:11]
	v_and_b32_e32 v0, 28, v195
	v_lshlrev_b32_e32 v0, 2, v0
	v_mov_b32_e32 v1, 0
	v_lshl_add_u64 v[96:97], v[2:3], 0, v[0:1]
	s_mov_b32 s3, 0x8000
	v_add_co_u32_e32 v2, vcc, s3, v96
	s_mov_b32 s5, 0x10000
	s_nop 0
	v_addc_co_u32_e32 v3, vcc, 0, v97, vcc
	global_load_dwordx4 v[52:55], v[96:97], off nt
	global_load_dwordx4 v[60:63], v[2:3], off nt
	v_add_co_u32_e32 v2, vcc, s5, v96
	s_mov_b32 s3, 0x18000
	s_nop 0
	v_addc_co_u32_e32 v3, vcc, 0, v97, vcc
	v_add_co_u32_e32 v4, vcc, s3, v96
	s_mov_b32 s3, 0x40000
	s_nop 0
	v_addc_co_u32_e32 v5, vcc, 0, v97, vcc
	global_load_dwordx4 v[76:79], v[2:3], off nt
	global_load_dwordx4 v[64:67], v[4:5], off nt
	v_add_co_u32_e32 v2, vcc, s3, v96
	s_mov_b32 s3, 0x48000
	s_nop 0
	v_addc_co_u32_e32 v3, vcc, 0, v97, vcc
	v_add_co_u32_e32 v4, vcc, s3, v96
	s_mov_b32 s3, 0x50000
	s_nop 0
	v_addc_co_u32_e32 v5, vcc, 0, v97, vcc
	global_load_dwordx4 v[68:71], v[2:3], off nt
	global_load_dwordx4 v[72:75], v[4:5], off nt
	v_add_co_u32_e32 v2, vcc, s3, v96
	s_mov_b32 s3, 0x58000
	s_nop 0
	v_addc_co_u32_e32 v3, vcc, 0, v97, vcc
	v_add_co_u32_e32 v4, vcc, s3, v96
	v_and_b32_e32 v0, 12, v195
	s_nop 0
	v_addc_co_u32_e32 v5, vcc, 0, v97, vcc
	global_load_dwordx4 v[56:59], v[2:3], off nt
	global_load_dwordx4 v[48:51], v[4:5], off nt
	v_bitop3_b32 v0, v0, v197, v198 bitop3:0x36
	v_lshlrev_b32_e32 v0, 4, v0
	v_lshl_add_u32 v2, v196, 9, 0
	s_movk_i32 s10, 0x60
	v_xad_u32 v83, v0, s10, v2
	s_movk_i32 s10, 0x80
	v_xad_u32 v84, v0, s10, v2
	s_movk_i32 s10, 0xa0
	v_xad_u32 v85, v0, s10, v2
	s_movk_i32 s10, 0xc0
	v_xad_u32 v86, v0, s10, v2
	s_movk_i32 s10, 0xe0
	v_xad_u32 v87, v0, s10, v2
	s_lshl_b32 s10, s22, 8
	s_add_i32 s10, s10, 0
	s_lshl_b32 s11, s22, 12
	v_add_u32_e32 v98, s10, v195
	s_lshl_b32 s10, s22, 2
	s_add_i32 s11, s11, 0
	v_add_u32_e32 v80, v2, v0
	v_xad_u32 v81, v0, 32, v2
	v_xad_u32 v82, v0, 64, v2
	s_add_i32 s10, s10, 0
	v_lshl_add_u32 v0, v194, 4, s11
	s_mov_b32 s3, 0
	v_add_u32_e32 v88, 0x20000, v98
	s_add_i32 s10, s10, 0x20800
	v_add_u32_e32 v89, 0x18000, v0
	s_setprio 1
	v_add_u32_e32 v0, 0x8000, v80
	ds_read_b128 v[2:5], v0
	ds_read_b128 v[18:21], v0 offset:256
	ds_read_b128 v[22:25], v0 offset:16384
	ds_read_b128 v[34:37], v0 offset:16640
	v_add_u32_e32 v0, 0x8000, v81
	ds_read_b128 v[26:29], v0
	ds_read_b128 v[30:33], v0 offset:256
	ds_read_b128 v[38:41], v0 offset:16384
	ds_read_b128 v[42:45], v0 offset:16640
	s_waitcnt lgkmcnt(4)
	v_add_u32_e32 v0, 0x8000, v82
	v_mfma_f32_32x32x16_bf16 v[2:17], v[2:5], v[128:131], 0
	s_waitcnt lgkmcnt(0)
	v_mfma_f32_32x32x16_bf16 v[2:17], v[18:21], v[160:163], v[2:17]
	ds_read_b128 v[18:21], v0
	ds_read_b128 v[90:93], v0 offset:256
	ds_read_b128 v[100:103], v0 offset:16384
	ds_read_b128 v[104:107], v0 offset:16640
	s_waitcnt lgkmcnt(4)
	v_add_u32_e32 v0, 0x8000, v83
	v_mfma_f32_32x32x16_bf16 v[2:17], v[26:29], v[132:135], v[2:17]
	ds_read_b128 v[26:29], v0
	v_mfma_f32_32x32x16_bf16 v[2:17], v[30:33], v[164:167], v[2:17]
	ds_read_b128 v[30:33], v0 offset:256
	ds_read_b128 v[108:111], v0 offset:16384
	ds_read_b128 v[112:115], v0 offset:16640
	s_waitcnt lgkmcnt(4)
	v_add_u32_e32 v0, 0x8000, v84
	v_mfma_f32_32x32x16_bf16 v[2:17], v[18:21], v[136:139], v[2:17]
	ds_read_b128 v[18:21], v0
	v_mfma_f32_32x32x16_bf16 v[2:17], v[90:93], v[168:171], v[2:17]
	ds_read_b128 v[90:93], v0 offset:256
	ds_read_b128 v[116:119], v0 offset:16384
	ds_read_b128 v[120:123], v0 offset:16640
	s_waitcnt lgkmcnt(4)
	v_add_u32_e32 v0, 0x8000, v85
	v_mfma_f32_32x32x16_bf16 v[2:17], v[26:29], v[140:143], v[2:17]
	ds_read_b128 v[26:29], v0
	v_mfma_f32_32x32x16_bf16 v[2:17], v[30:33], v[172:175], v[2:17]
	ds_read_b128 v[30:33], v0 offset:256
	ds_read_b128 v[124:127], v0 offset:16384
	ds_read_b128 v[194:197], v0 offset:16640
	s_waitcnt lgkmcnt(4)
	v_add_u32_e32 v0, 0x8000, v86
	v_mfma_f32_32x32x16_bf16 v[2:17], v[18:21], v[144:147], v[2:17]
	ds_read_b128 v[18:21], v0
	v_mfma_f32_32x32x16_bf16 v[2:17], v[90:93], v[176:179], v[2:17]
	ds_read_b128 v[90:93], v0 offset:256
	ds_read_b128 v[198:201], v0 offset:16384
	ds_read_b128 v[202:205], v0 offset:16640
	s_waitcnt lgkmcnt(4)
	v_add_u32_e32 v0, 0x8000, v87
	v_mfma_f32_32x32x16_bf16 v[2:17], v[26:29], v[148:151], v[2:17]
	ds_read_b128 v[26:29], v0
	v_mfma_f32_32x32x16_bf16 v[2:17], v[30:33], v[180:183], v[2:17]
	ds_read_b128 v[30:33], v0 offset:256
	ds_read_b128 v[206:209], v0 offset:16384
	ds_read_b128 v[210:213], v0 offset:16640
	s_waitcnt lgkmcnt(4)
	s_nop 0
	s_waitcnt lgkmcnt(0)
	v_mfma_f32_32x32x16_bf16 v[2:17], v[18:21], v[152:155], v[2:17]
	v_mfma_f32_32x32x16_bf16 v[2:17], v[90:93], v[184:187], v[2:17]
	v_mfma_f32_32x32x16_bf16 v[2:17], v[26:29], v[156:159], v[2:17]
	v_mfma_f32_32x32x16_bf16 v[2:17], v[30:33], v[188:191], v[2:17]
	s_setprio 0
	v_mfma_f32_32x32x16_bf16 v[18:33], v[22:25], v[128:131], 0
	s_nop 9
	v_max_f32_e32 v0, v3, v3
	ds_write_b32 v88, v1
	v_mov_b32_e32 v1, 1
	s_mov_b32 s11, 1
	s_mov_b32 s12, 0x41300000
	v_mfma_f32_32x32x16_bf16 v[18:33], v[34:37], v[160:163], v[18:33]
	v_max_f32_e32 v34, v2, v2
	v_max_f32_e32 v0, v34, v0
	v_max3_f32 v0, v0, v4, v5
	v_max3_f32 v0, v0, v6, v7
	v_max3_f32 v0, v0, v8, v9
	v_max3_f32 v0, v0, v10, v11
	v_max3_f32 v0, v0, v12, v13
	v_mfma_f32_32x32x16_bf16 v[18:33], v[38:41], v[132:135], v[18:33]
	v_max3_f32 v0, v0, v14, v15
	v_max3_f32 v0, v0, v16, v17
	v_mov_b32_e32 v34, s10
	ds_write_b32 v34, v1
	v_mfma_f32_32x32x16_bf16 v[18:33], v[42:45], v[164:167], v[18:33]
	v_mfma_f32_32x32x16_bf16 v[18:33], v[100:103], v[136:139], v[18:33]
	v_mfma_f32_32x32x16_bf16 v[18:33], v[104:107], v[168:171], v[18:33]
	v_mfma_f32_32x32x16_bf16 v[18:33], v[108:111], v[140:143], v[18:33]
	v_mfma_f32_32x32x16_bf16 v[18:33], v[112:115], v[172:175], v[18:33]
	v_mfma_f32_32x32x16_bf16 v[18:33], v[116:119], v[144:147], v[18:33]
	v_mfma_f32_32x32x16_bf16 v[18:33], v[120:123], v[176:179], v[18:33]
	v_mfma_f32_32x32x16_bf16 v[18:33], v[124:127], v[148:151], v[18:33]
	v_mfma_f32_32x32x16_bf16 v[18:33], v[194:197], v[180:183], v[18:33]
	v_mfma_f32_32x32x16_bf16 v[18:33], v[198:201], v[152:155], v[18:33]
	v_mfma_f32_32x32x16_bf16 v[18:33], v[202:205], v[184:187], v[18:33]
	v_mfma_f32_32x32x16_bf16 v[18:33], v[206:209], v[156:159], v[18:33]
	v_mfma_f32_32x32x16_bf16 v[18:33], v[210:213], v[188:191], v[18:33]
	s_nop 11
	v_max3_f32 v0, v0, v18, v19
	v_max3_f32 v0, v0, v20, v21
	v_max3_f32 v0, v0, v22, v23
	v_max3_f32 v0, v0, v24, v25
	v_max3_f32 v0, v0, v26, v27
	v_max3_f32 v0, v0, v28, v29
	v_max3_f32 v0, v0, v30, v31
	v_max3_f32 v0, v0, v32, v33
	v_mov_b32_e32 v1, v0
	s_nop 1
	v_permlane32_swap_b32_e32 v0, v1
	v_max_f32_e32 v1, v1, v1
	v_max_f32_e32 v0, v0, v0
	v_max_f32_e32 v0, v0, v1
	v_add_f32_e32 v90, 0, v0
	v_add_f32_e64 v2, -v90, v2
	v_add_f32_e64 v3, -v90, v3
	v_add_f32_e64 v4, -v90, v4
	v_add_f32_e64 v5, -v90, v5
	v_add_f32_e64 v6, -v90, v6
	v_add_f32_e64 v7, -v90, v7
	v_add_f32_e64 v8, -v90, v8
	v_add_f32_e64 v9, -v90, v9
	v_add_f32_e64 v1, -v90, v18
	v_add_f32_e64 v18, -v90, v19
	v_add_f32_e64 v19, -v90, v20
	v_add_f32_e64 v20, -v90, v21
	v_add_f32_e64 v21, -v90, v22
	v_add_f32_e64 v22, -v90, v23
	v_add_f32_e64 v23, -v90, v24
	v_add_f32_e64 v24, -v90, v25
	v_add_f32_e64 v25, -v90, v26
	v_add_f32_e64 v26, -v90, v27
	v_add_f32_e64 v27, -v90, v28
	v_add_f32_e64 v28, -v90, v29
	v_add_f32_e64 v29, -v90, v30
	v_add_f32_e64 v30, -v90, v31
	v_add_f32_e64 v31, -v90, v32
	v_add_f32_e64 v32, -v90, v33
	v_add_f32_e64 v10, -v90, v10
	v_add_f32_e64 v11, -v90, v11
	v_add_f32_e64 v12, -v90, v12
	v_add_f32_e64 v13, -v90, v13
	v_add_f32_e64 v14, -v90, v14
	v_add_f32_e64 v15, -v90, v15
	v_add_f32_e64 v16, -v90, v16
	v_add_f32_e64 v17, -v90, v17
	v_exp_f32_e32 v33, v2
	v_exp_f32_e32 v34, v3
	v_exp_f32_e32 v35, v4
	v_exp_f32_e32 v36, v5
	v_exp_f32_e32 v37, v6
	v_exp_f32_e32 v38, v7
	v_exp_f32_e32 v39, v8
	v_exp_f32_e32 v40, v9
	v_exp_f32_e32 v41, v10
	v_exp_f32_e32 v42, v11
	v_exp_f32_e32 v43, v12
	v_exp_f32_e32 v44, v13
	v_exp_f32_e32 v45, v14
	v_exp_f32_e32 v46, v15
	v_exp_f32_e32 v47, v16
	v_exp_f32_e32 v91, v17
	v_exp_f32_e32 v92, v1
	v_exp_f32_e32 v93, v18
	v_exp_f32_e32 v94, v19
	v_exp_f32_e32 v95, v20
	v_exp_f32_e32 v99, v21
	v_exp_f32_e32 v100, v22
	v_exp_f32_e32 v101, v23
	v_exp_f32_e32 v102, v24
	v_exp_f32_e32 v103, v25
	v_exp_f32_e32 v104, v26
	v_exp_f32_e32 v105, v27
	v_exp_f32_e32 v28, v28
	v_exp_f32_e32 v29, v29
	v_exp_f32_e32 v30, v30
	v_exp_f32_e32 v31, v31
	v_exp_f32_e32 v32, v32
	v_cvt_pk_bf16_f32 v12, v33, v34
	v_cvt_pk_bf16_f32 v13, v35, v36
	v_cvt_pk_bf16_f32 v14, v37, v38
	v_cvt_pk_bf16_f32 v15, v39, v40
	v_add_f32_e32 v33, 0, v33
	v_cvt_pk_bf16_f32 v16, v41, v42
	v_cvt_pk_bf16_f32 v17, v43, v44
	v_cvt_pk_bf16_f32 v18, v45, v46
	v_cvt_pk_bf16_f32 v19, v47, v91
	v_cvt_pk_bf16_f32 v20, v92, v93
	v_cvt_pk_bf16_f32 v21, v94, v95
	v_cvt_pk_bf16_f32 v22, v99, v100
	v_cvt_pk_bf16_f32 v23, v101, v102
	v_cvt_pk_bf16_f32 v24, v103, v104
	v_cvt_pk_bf16_f32 v25, v105, v28
	v_cvt_pk_bf16_f32 v26, v29, v30
	v_cvt_pk_bf16_f32 v27, v31, v32
	ds_write_b128 v89, v[12:15]
	ds_write_b128 v89, v[16:19] offset:1024
	ds_write_b128 v89, v[20:23] offset:2048
	ds_write_b128 v89, v[24:27] offset:3072
	v_add_f32_e32 v12, v33, v34
	v_add_f32_e32 v12, v12, v35
	v_add_f32_e32 v12, v12, v36
	v_add_f32_e32 v12, v12, v37
	v_add_f32_e32 v12, v12, v38
	v_add_f32_e32 v12, v12, v39
	v_add_f32_e32 v12, v12, v40
	v_add_f32_e32 v12, v12, v41
	v_add_f32_e32 v12, v12, v42
	v_add_f32_e32 v12, v12, v43
	v_add_f32_e32 v12, v12, v44
	v_add_f32_e32 v12, v12, v45
	v_add_f32_e32 v12, v12, v46
	v_add_f32_e32 v12, v12, v47
	v_add_f32_e32 v12, v12, v91
	v_add_f32_e32 v12, v12, v92
	v_add_f32_e32 v12, v12, v93
	v_add_f32_e32 v12, v12, v94
	v_add_f32_e32 v12, v12, v95
	v_add_f32_e32 v12, v12, v99
	v_add_f32_e32 v12, v12, v100
	v_add_f32_e32 v12, v12, v101
	v_add_f32_e32 v12, v12, v102
	v_add_f32_e32 v12, v12, v103
	v_add_f32_e32 v12, v12, v104
	v_add_f32_e32 v12, v12, v105
	v_add_f32_e32 v12, v12, v28
	v_add_f32_e32 v12, v12, v29
	v_add_f32_e32 v12, v12, v30
	s_waitcnt vmcnt(8) lgkmcnt(0)
	s_barrier
	v_add_f32_e32 v12, v12, v31
	v_xor_b32_e32 v0, 0x80000000, v90
	v_add_f32_e32 v12, v12, v32
	v_mov_b32_e32 v1, v0
	v_mov_b32_e32 v2, v0
	v_mov_b32_e32 v3, v0
	v_mov_b32_e32 v4, v0
	v_mov_b32_e32 v5, v0
	v_mov_b32_e32 v6, v0
	v_mov_b32_e32 v7, v0
	v_mov_b32_e32 v8, v0
	v_mov_b32_e32 v9, v0
	v_mov_b32_e32 v10, v0
	v_mov_b32_e32 v11, v0
	v_add_f32_e32 v99, 0, v12
	v_mov_b32_e32 v12, v0
	v_mov_b32_e32 v13, v0
	v_mov_b32_e32 v14, v0
	v_mov_b32_e32 v15, v0
	s_branch .LBB1_21
